# speedup vs baseline: 1.0191x; 1.0048x over previous
.LBB2_35:
	s_or_b64 exec, exec, s[8:9]
	v_cvt_f32_i32_e32 v38, v35
	v_cvt_f32_f16_sdwa v40, v7 dst_sel:DWORD dst_unused:UNUSED_PAD src0_sel:WORD_1
	v_cvt_f32_f16_e32 v39, v3
	v_cvt_f32_f16_e32 v43, v11
	v_max_f32_e32 v7, 1.0, v38
	v_div_scale_f32 v38, s[8:9], v7, v7, 1.0
	v_rcp_f32_e32 v42, v38
	v_div_scale_f32 v44, vcc, 1.0, v7, 1.0
	s_waitcnt vmcnt(1)
	v_add_f32_e32 v22, v22, v18
	v_fma_f32 v45, -v38, v42, 1.0
	v_fmac_f32_e32 v42, v45, v42
	v_mul_f32_e32 v45, v44, v42
	v_fma_f32 v46, -v38, v45, v44
	v_fmac_f32_e32 v45, v46, v42
	v_fma_f32 v38, -v38, v45, v44
	v_add_f32_e32 v37, 0, v37
	v_add_f32_e32 v22, v22, v39
	v_add_f32_e32 v26, v26, v18
	v_div_fmas_f32 v38, v38, v42, v45
	v_cndmask_b32_e64 v37, 0, v37, s[2:3]
	v_mul_f32_e32 v42, 0x3e4ccccd, v22
	v_cmp_lt_f32_e32 vcc, 0, v22
	v_cndmask_b32_e64 v39, 0, v39, s[4:5]
	v_add_f32_e32 v26, v26, v43
	v_cndmask_b32_e32 v22, v42, v22, vcc
	v_add_f32_e32 v37, v37, v39
	v_mul_f32_e32 v39, 0x3e4ccccd, v26
	v_cmp_lt_f32_e32 vcc, 0, v26
	v_div_fixup_f32 v7, v38, v7, 1.0
	v_max_f32_e32 v38, v13, v13
	v_cndmask_b32_e32 v26, v39, v26, vcc
	v_cndmask_b32_e64 v39, 0, v43, s[6:7]
	v_max_f32_e32 v38, 0xff800000, v38
	v_cndmask_b32_e64 v22, v5, v22, s[4:5]
	v_cndmask_b32_e64 v26, v5, v26, s[6:7]
	v_add_f32_e32 v37, v37, v39
	v_max3_f32 v44, v38, v22, v26
	s_waitcnt vmcnt(0)
	v_mov_b32_e32 v42, v14
	v_add_f32_e32 v23, v23, v19
	v_add_f32_dpp v37, v37, v37 quad_perm:[1,0,3,2] row_mask:0xf bank_mask:0xf
	v_add_f32_e32 v24, v24, v20
	s_nop 0
	v_add_f32_dpp v37, v37, v37 quad_perm:[2,3,0,1] row_mask:0xf bank_mask:0xf
	s_nop 1
	v_add_f32_dpp v39, v37, v37 row_half_mirror row_mask:0xf bank_mask:0xf
	v_mov_b32_e32 v38, v18
	v_mov_b32_e32 v43, v39
	s_nop 0
	v_max_f32_dpp v18, v44, v44 quad_perm:[1,0,3,2] row_mask:0xf bank_mask:0xf
	v_mov_b32_dpp v43, v43 row_mirror row_mask:0xf bank_mask:0xf
	v_pk_add_f32 v[38:39], v[38:39], v[42:43]
	v_max_f32_dpp v18, v18, v18 quad_perm:[2,3,0,1] row_mask:0xf bank_mask:0xf
	v_fmac_f32_e32 v38, v7, v39
	v_mul_f32_e32 v14, 0x3e4ccccd, v38
	v_max_f32_dpp v18, v18, v18 row_half_mirror row_mask:0xf bank_mask:0xf
	v_cmp_lt_f32_e32 vcc, 0, v38
	v_cvt_f32_f16_sdwa v42, v11 dst_sel:DWORD dst_unused:UNUSED_PAD src0_sel:WORD_1
	s_nop 0
	v_cndmask_b32_e32 v14, v14, v38, vcc
	v_max_f32_dpp v37, v18, v18 row_mirror row_mask:0xf bank_mask:0xf
	v_max_f32_e32 v37, v37, v14
	v_sub_f32_e32 v13, v13, v37
	v_mul_f32_e32 v13, 0x3fb8aa3b, v13
	v_sub_f32_e32 v11, v22, v37
	v_exp_f32_e32 v13, v13
	v_mul_f32_e32 v11, 0x3fb8aa3b, v11
	v_sub_f32_e32 v18, v26, v37
	v_exp_f32_e32 v11, v11
	v_mul_f32_e32 v18, 0x3fb8aa3b, v18
	v_exp_f32_e32 v18, v18
	v_cvt_f32_f16_sdwa v39, v3 dst_sel:DWORD dst_unused:UNUSED_PAD src0_sel:WORD_1
	v_add_f32_e32 v3, 0, v13
	v_cndmask_b32_e64 v3, 0, v3, s[2:3]
	v_cndmask_b32_e64 v22, 0, v11, s[4:5]
	v_add_f32_e32 v3, v22, v3
	v_cndmask_b32_e64 v22, 0, v18, s[6:7]
	v_sub_f32_e32 v14, v14, v37
	v_add_f32_e32 v3, v22, v3
	v_mul_f32_e32 v14, 0x3fb8aa3b, v14
	v_exp_f32_e32 v37, v14
	v_add_f32_e32 v23, v23, v39
	v_mul_f32_e32 v26, 0x3e4ccccd, v23
	v_add_f32_dpp v3, v3, v3 quad_perm:[1,0,3,2] row_mask:0xf bank_mask:0xf
	v_cvt_f32_f16_e32 v38, v8
	s_nop 0
	v_add_f32_dpp v3, v3, v3 quad_perm:[2,3,0,1] row_mask:0xf bank_mask:0xf
	s_nop 1
	v_add_f32_dpp v3, v3, v3 row_half_mirror row_mask:0xf bank_mask:0xf
	s_nop 1
	v_add_f32_dpp v3, v3, v3 row_mirror row_mask:0xf bank_mask:0xf
	v_add_f32_e32 v14, v30, v19
	v_add_f32_e32 v14, v14, v40
	v_mul_f32_e32 v22, 0x3e4ccccd, v14
	v_cmp_lt_f32_e32 vcc, 0, v14
	v_add_f32_e32 v3, v37, v3
	v_add_f32_e32 v3, 0x24e69595, v3
	v_cndmask_b32_e32 v14, v22, v14, vcc
	v_cmp_lt_f32_e32 vcc, 0, v23
	v_add_f32_e32 v22, 0, v40
	v_cndmask_b32_e64 v22, 0, v22, s[2:3]
	v_cndmask_b32_e32 v23, v26, v23, vcc
	v_cndmask_b32_e64 v26, 0, v39, s[4:5]
	v_cndmask_b32_e64 v39, v5, v23, s[4:5]
	v_add_f32_e32 v23, v27, v19
	v_add_f32_e32 v23, v23, v42
	v_add_f32_e32 v22, v22, v26
	v_mul_f32_e32 v26, 0x3e4ccccd, v23
	v_cmp_lt_f32_e32 vcc, 0, v23
	v_cndmask_b32_e64 v30, v5, v14, s[2:3]
	v_max_f32_e32 v14, 0xff800000, v30
	v_cndmask_b32_e32 v23, v26, v23, vcc
	v_cndmask_b32_e64 v26, 0, v42, s[6:7]
	v_cndmask_b32_e64 v40, v5, v23, s[6:7]
	v_max3_f32 v42, v14, v39, v40
	v_add_f32_e32 v14, v22, v26
	v_mov_b32_e32 v26, v15
	v_rcp_f32_e32 v3, v3
	v_add_f32_dpp v14, v14, v14 quad_perm:[1,0,3,2] row_mask:0xf bank_mask:0xf
	s_nop 1
	v_add_f32_dpp v14, v14, v14 quad_perm:[2,3,0,1] row_mask:0xf bank_mask:0xf
	s_nop 1
	v_add_f32_dpp v23, v14, v14 row_half_mirror row_mask:0xf bank_mask:0xf
	v_mov_b32_e32 v27, v23
	v_mov_b32_e32 v22, v19
	s_nop 0
	v_mov_b32_dpp v27, v27 row_mirror row_mask:0xf bank_mask:0xf
	v_pk_add_f32 v[14:15], v[22:23], v[26:27]
	v_mul_f32_e32 v22, v37, v3
	v_fmac_f32_e32 v14, v7, v15
	v_mul_f32_e32 v15, 0x3e4ccccd, v14
	v_cmp_lt_f32_e32 vcc, 0, v14
	v_cvt_f32_f16_e32 v27, v4
	v_add_f32_e32 v24, v24, v27
	v_cndmask_b32_e32 v14, v15, v14, vcc
	v_cndmask_b32_e64 v27, 0, v27, s[4:5]
	s_nop 0
	v_max_f32_dpp v15, v42, v42 quad_perm:[1,0,3,2] row_mask:0xf bank_mask:0xf
	s_nop 1
	v_max_f32_dpp v15, v15, v15 quad_perm:[2,3,0,1] row_mask:0xf bank_mask:0xf
	s_nop 1
	v_max_f32_dpp v15, v15, v15 row_half_mirror row_mask:0xf bank_mask:0xf
	s_nop 1
	v_max_f32_dpp v19, v15, v15 row_mirror row_mask:0xf bank_mask:0xf
	v_max_f32_e32 v15, v19, v14
	v_sub_f32_e32 v19, v30, v15
	v_mul_f32_e32 v19, 0x3fb8aa3b, v19
	v_exp_f32_e32 v23, v19
	v_sub_f32_e32 v19, v39, v15
	v_mul_f32_e32 v19, 0x3fb8aa3b, v19
	v_sub_f32_e32 v26, v40, v15
	v_exp_f32_e32 v19, v19
	v_mul_f32_e32 v26, 0x3fb8aa3b, v26
	v_exp_f32_e32 v26, v26
	v_add_f32_e32 v37, 0, v23
	v_cndmask_b32_e64 v37, 0, v37, s[2:3]
	v_cndmask_b32_e64 v39, 0, v19, s[4:5]
	v_add_f32_e32 v37, v39, v37
	v_cndmask_b32_e64 v39, 0, v26, s[6:7]
	v_sub_f32_e32 v14, v14, v15
	v_add_f32_e32 v37, v39, v37
	v_mul_f32_e32 v14, 0x3fb8aa3b, v14
	v_exp_f32_e32 v39, v14
	v_cvt_f32_f16_e32 v30, v12
	s_nop 0
	v_add_f32_dpp v14, v37, v37 quad_perm:[1,0,3,2] row_mask:0xf bank_mask:0xf
	s_nop 1
	v_add_f32_dpp v14, v14, v14 quad_perm:[2,3,0,1] row_mask:0xf bank_mask:0xf
	s_nop 1
	v_add_f32_dpp v14, v14, v14 row_half_mirror row_mask:0xf bank_mask:0xf
	s_nop 1
	v_add_f32_dpp v37, v14, v14 row_mirror row_mask:0xf bank_mask:0xf
	v_add_f32_e32 v14, v31, v20
	v_add_f32_e32 v14, v14, v38
	v_mul_f32_e32 v15, 0x3e4ccccd, v14
	v_cmp_lt_f32_e32 vcc, 0, v14
	v_mul_f32_e32 v31, 0x3e4ccccd, v24
	s_nop 0
	v_cndmask_b32_e32 v14, v15, v14, vcc
	v_cmp_lt_f32_e32 vcc, 0, v24
	v_add_f32_e32 v15, 0, v38
	v_cndmask_b32_e64 v15, 0, v15, s[2:3]
	v_cndmask_b32_e32 v24, v31, v24, vcc
	v_cndmask_b32_e64 v38, v5, v24, s[4:5]
	v_add_f32_e32 v24, v28, v20
	v_add_f32_e32 v24, v24, v30
	v_add_f32_e32 v15, v15, v27
	v_mul_f32_e32 v27, 0x3e4ccccd, v24
	v_cmp_lt_f32_e32 vcc, 0, v24
	v_cndmask_b32_e64 v40, v5, v14, s[2:3]
	v_max_f32_e32 v14, 0xff800000, v40
	v_cndmask_b32_e32 v24, v27, v24, vcc
	v_cndmask_b32_e64 v27, 0, v30, s[6:7]
	v_cndmask_b32_e64 v28, v5, v24, s[6:7]
	v_max3_f32 v24, v14, v38, v28
	v_add_f32_e32 v14, v15, v27
	v_mov_b32_e32 v30, v16
	s_nop 0
	v_add_f32_dpp v14, v14, v14 quad_perm:[1,0,3,2] row_mask:0xf bank_mask:0xf
	s_nop 1
	v_add_f32_dpp v14, v14, v14 quad_perm:[2,3,0,1] row_mask:0xf bank_mask:0xf
	s_nop 1
	v_add_f32_dpp v15, v14, v14 row_half_mirror row_mask:0xf bank_mask:0xf
	v_mov_b32_e32 v31, v15
	v_mov_b32_e32 v14, v20
	s_nop 0
	v_mov_b32_dpp v31, v31 row_mirror row_mask:0xf bank_mask:0xf
	v_pk_add_f32 v[14:15], v[14:15], v[30:31]
	s_nop 0
	v_fmac_f32_e32 v14, v7, v15
	v_mul_f32_e32 v15, 0x3e4ccccd, v14
	v_cmp_lt_f32_e32 vcc, 0, v14
	s_nop 1
	v_cndmask_b32_e32 v14, v15, v14, vcc
	v_cmp_eq_u32_e32 vcc, v33, v35
	s_nop 0
	v_max_f32_dpp v15, v24, v24 quad_perm:[1,0,3,2] row_mask:0xf bank_mask:0xf
	s_nop 1
	v_max_f32_dpp v15, v15, v15 quad_perm:[2,3,0,1] row_mask:0xf bank_mask:0xf
	s_nop 1
	v_max_f32_dpp v15, v15, v15 row_half_mirror row_mask:0xf bank_mask:0xf
	s_nop 1
	v_max_f32_dpp v16, v15, v15 row_mirror row_mask:0xf bank_mask:0xf
	v_max_f32_e32 v15, v16, v14
	v_sub_f32_e32 v16, v40, v15
	v_mul_f32_e32 v16, 0x3fb8aa3b, v16
	v_sub_f32_e32 v20, v38, v15
	v_exp_f32_e32 v24, v16
	v_mul_f32_e32 v20, 0x3fb8aa3b, v20
	v_sub_f32_e32 v28, v28, v15
	v_exp_f32_e32 v20, v20
	v_mul_f32_e32 v28, 0x3fb8aa3b, v28
	v_add_f32_e32 v16, v39, v37
	v_exp_f32_e32 v37, v28
	v_add_f32_e32 v16, 0x24e69595, v16
	v_rcp_f32_e32 v27, v16
	v_add_f32_e32 v16, 0, v24
	v_cndmask_b32_e64 v16, 0, v16, s[2:3]
	v_cndmask_b32_e64 v28, 0, v20, s[4:5]
	v_add_f32_e32 v16, v28, v16
	v_cndmask_b32_e64 v28, 0, v37, s[6:7]
	v_sub_f32_e32 v14, v14, v15
	v_add_f32_e32 v16, v28, v16
	v_mul_f32_e32 v14, 0x3fb8aa3b, v14
	v_exp_f32_e32 v28, v14
	v_mul_f32_e32 v30, v39, v27
	s_nop 0
	v_add_f32_dpp v14, v16, v16 quad_perm:[1,0,3,2] row_mask:0xf bank_mask:0xf
	s_nop 1
	v_add_f32_dpp v14, v14, v14 quad_perm:[2,3,0,1] row_mask:0xf bank_mask:0xf
	s_nop 1
	v_add_f32_dpp v14, v14, v14 row_half_mirror row_mask:0xf bank_mask:0xf
	s_nop 1
	v_add_f32_dpp v14, v14, v14 row_mirror row_mask:0xf bank_mask:0xf
	v_add_f32_e32 v14, v28, v14
	v_add_f32_e32 v14, 0x24e69595, v14
	v_rcp_f32_e32 v31, v14
	v_cndmask_b32_e32 v14, 0, v22, vcc
	v_cndmask_b32_e32 v15, 0, v30, vcc
	v_mul_f32_e32 v33, v28, v31
	v_cndmask_b32_e32 v16, 0, v33, vcc
	v_mov_b32_e32 v28, 0
	s_and_saveexec_b64 s[10:11], s[6:7]
	s_cbranch_execz .LBB2_37
	v_cvt_f32_f16_sdwa v28, v12 dst_sel:DWORD dst_unused:UNUSED_PAD src0_sel:WORD_1
	v_add_f32_e32 v5, v29, v21
	v_mul_f32_e32 v16, v37, v31
	v_mul_f32_e32 v15, v26, v27
	v_add_f32_e32 v5, v5, v28
	v_mul_f32_e32 v12, 0x3e4ccccd, v5
	v_cmp_lt_f32_e64 s[8:9], 0, v5
	v_mul_f32_e32 v14, v18, v3
	s_nop 0
	v_cndmask_b32_e64 v5, v12, v5, s[8:9]
.LBB2_37:
	s_or_b64 exec, exec, s[10:11]
	v_cvt_f32_f16_sdwa v8, v8 dst_sel:DWORD dst_unused:UNUSED_PAD src0_sel:WORD_1
	v_cvt_f32_f16_sdwa v4, v4 dst_sel:DWORD dst_unused:UNUSED_PAD src0_sel:WORD_1
	v_add_f32_e32 v12, v32, v21
	v_add_f32_e32 v25, v25, v21
	v_add_f32_e32 v12, v12, v8
	v_mul_f32_e32 v18, 0x3e4ccccd, v12
	v_cmp_lt_f32_e64 s[8:9], 0, v12
	v_add_f32_e32 v25, v25, v4
	v_mul_f32_e32 v26, 0x3e4ccccd, v25
	v_cndmask_b32_e64 v12, v18, v12, s[8:9]
	v_cmp_lt_f32_e64 s[8:9], 0, v25
	v_mov_b32_e32 v18, 0xff800000
	v_cndmask_b32_e64 v12, v18, v12, s[2:3]
	v_cndmask_b32_e64 v25, v26, v25, s[8:9]
	v_cmp_eq_u32_e64 s[8:9], v9, v35
	v_cndmask_b32_e64 v25, v18, v25, s[4:5]
	v_add_f32_e32 v8, 0, v8
	v_mul_f32_e32 v18, v20, v31
	v_cndmask_b32_e64 v9, 0, v33, s[8:9]
	v_cmp_eq_u32_e64 s[10:11], v69, v35
	v_cndmask_b32_e64 v4, 0, v4, s[4:5]
	v_cndmask_b32_e64 v8, 0, v8, s[2:3]
	v_cndmask_b32_e64 v20, v9, v18, s[4:5]
	v_mul_f32_e32 v9, v24, v31
	v_cndmask_b32_e64 v18, 0, v33, s[10:11]
	v_add_f32_e32 v4, v8, v4
	v_cndmask_b32_e64 v24, v18, v9, s[2:3]
	v_mul_f32_e32 v9, v19, v27
	v_cndmask_b32_e64 v18, 0, v30, s[8:9]
	v_max_f32_e32 v8, 0xff800000, v12
	v_cndmask_b32_e64 v19, v18, v9, s[4:5]
	v_mul_f32_e32 v9, v23, v27
	v_cndmask_b32_e64 v18, 0, v30, s[10:11]
	v_add_f32_e32 v4, v4, v28
	v_cndmask_b32_e64 v23, v18, v9, s[2:3]
	v_max3_f32 v18, v8, v25, v5
	v_mov_b32_e32 v26, v17
	v_lshlrev_b32_e32 v71, 4, v69
	v_add_f32_dpp v4, v4, v4 quad_perm:[1,0,3,2] row_mask:0xf bank_mask:0xf
	s_nop 1
	v_add_f32_dpp v4, v4, v4 quad_perm:[2,3,0,1] row_mask:0xf bank_mask:0xf
	s_nop 1
	v_add_f32_dpp v9, v4, v4 row_half_mirror row_mask:0xf bank_mask:0xf
	v_mov_b32_e32 v27, v9
	v_mov_b32_e32 v8, v21
	s_nop 0
	v_mov_b32_dpp v27, v27 row_mirror row_mask:0xf bank_mask:0xf
	v_pk_add_f32 v[8:9], v[8:9], v[26:27]
	s_nop 0
	v_fmac_f32_e32 v8, v7, v9
	v_mul_f32_e32 v4, 0x3e4ccccd, v8
	v_cmp_lt_f32_e64 s[12:13], 0, v8
	v_max_f32_dpp v7, v18, v18 quad_perm:[1,0,3,2] row_mask:0xf bank_mask:0xf
	s_nop 0
	v_cndmask_b32_e64 v4, v4, v8, s[12:13]
	v_mul_f32_e32 v9, v11, v3
	v_cndmask_b32_e64 v11, 0, v22, s[8:9]
	v_max_f32_dpp v7, v7, v7 quad_perm:[2,3,0,1] row_mask:0xf bank_mask:0xf
	v_cndmask_b32_e64 v18, v11, v9, s[4:5]
	v_mul_f32_e32 v3, v13, v3
	v_max_f32_dpp v7, v7, v7 row_half_mirror row_mask:0xf bank_mask:0xf
	s_nop 1
	v_max_f32_dpp v8, v7, v7 row_mirror row_mask:0xf bank_mask:0xf
	v_max_f32_e32 v7, v8, v4
	v_sub_f32_e32 v8, v12, v7
	v_mul_f32_e32 v8, 0x3fb8aa3b, v8
	v_sub_f32_e32 v11, v25, v7
	v_exp_f32_e32 v8, v8
	v_mul_f32_e32 v11, 0x3fb8aa3b, v11
	v_sub_f32_e32 v5, v5, v7
	v_exp_f32_e32 v11, v11
	v_mul_f32_e32 v5, 0x3fb8aa3b, v5
	v_exp_f32_e32 v5, v5
	v_add_f32_e32 v9, 0, v8
	v_cndmask_b32_e64 v9, 0, v9, s[2:3]
	v_cndmask_b32_e64 v12, 0, v11, s[4:5]
	v_add_f32_e32 v9, v12, v9
	v_cndmask_b32_e64 v12, 0, v5, s[6:7]
	v_add_f32_e32 v9, v12, v9
	v_sub_f32_e32 v4, v4, v7
	v_mul_f32_e32 v4, 0x3fb8aa3b, v4
	v_exp_f32_e32 v4, v4
	v_add_f32_dpp v7, v9, v9 quad_perm:[1,0,3,2] row_mask:0xf bank_mask:0xf
	s_nop 1
	v_add_f32_dpp v7, v7, v7 quad_perm:[2,3,0,1] row_mask:0xf bank_mask:0xf
	s_nop 1
	v_add_f32_dpp v7, v7, v7 row_half_mirror row_mask:0xf bank_mask:0xf
	s_nop 1
	v_add_f32_dpp v7, v7, v7 row_mirror row_mask:0xf bank_mask:0xf
	v_add_f32_e32 v7, v4, v7
	v_add_f32_e32 v7, 0x24e69595, v7
	v_rcp_f32_e32 v7, v7
	v_cndmask_b32_e64 v9, 0, v22, s[10:11]
	v_cndmask_b32_e64 v22, v9, v3, s[2:3]
	v_mul_f32_e32 v3, v4, v7
	v_mul_f32_e32 v4, v8, v7
	v_cndmask_b32_e64 v8, 0, v3, s[10:11]
	v_cndmask_b32_e64 v25, v8, v4, s[2:3]
	v_mul_f32_e32 v4, v11, v7
	v_cndmask_b32_e64 v8, 0, v3, s[8:9]
	v_cndmask_b32_e64 v21, v8, v4, s[4:5]
	s_movk_i32 s4, 0x410
	v_mul_f32_e32 v4, v5, v7
	v_cndmask_b32_e32 v3, 0, v3, vcc
	v_mul_lo_u32 v70, v41, s4
	v_cndmask_b32_e64 v17, v3, v4, s[6:7]
	v_add_u32_e32 v3, v70, v71
	ds_write_b128 v3, v[22:25]
	v_lshl_add_u32 v4, v69, 2, v70
	ds_write_b128 v3, v[18:21] offset:256
	ds_write2_b32 v4, v6, v2 offset0:192 offset1:208
	ds_write_b128 v3, v[14:17] offset:512
	ds_write_b32 v4, v10 offset:896
	s_branch .LBB2_48

.LBB2_45:
	s_or_b64 exec, exec, s[6:7]
	v_cvt_f32_i32_e32 v26, v35
	v_cvt_f32_f16_sdwa v32, v7 dst_sel:DWORD dst_unused:UNUSED_PAD src0_sel:WORD_1
	v_cvt_f32_f16_e32 v30, v3
	s_waitcnt vmcnt(1)
	v_add_f32_e32 v18, v18, v14
	v_max_f32_e32 v7, 1.0, v26
	v_div_scale_f32 v26, s[6:7], v7, v7, 1.0
	v_rcp_f32_e32 v27, v26
	v_div_scale_f32 v31, vcc, 1.0, v7, 1.0
	v_add_f32_e32 v18, v18, v30
	v_fma_f32 v33, -v26, v27, 1.0
	v_fmac_f32_e32 v27, v33, v27
	v_mul_f32_e32 v33, v31, v27
	v_fma_f32 v36, -v26, v33, v31
	v_fmac_f32_e32 v33, v36, v27
	v_fma_f32 v26, -v26, v33, v31
	v_div_fmas_f32 v26, v26, v27, v33
	v_div_fixup_f32 v7, v26, v7, 1.0
	v_add_f32_e32 v26, 0, v29
	v_mul_f32_e32 v27, 0x3e4ccccd, v18
	v_cmp_lt_f32_e32 vcc, 0, v18
	v_cndmask_b32_e64 v26, 0, v26, s[2:3]
	s_mov_b32 s10, 0xff800000
	v_cndmask_b32_e32 v18, v27, v18, vcc
	v_cndmask_b32_e64 v27, 0, v30, s[4:5]
	v_add_f32_e32 v26, v26, v27
	s_waitcnt vmcnt(0)
	v_mov_b32_e32 v30, v10
	v_cndmask_b32_e64 v18, v5, v18, s[4:5]
	v_add_f32_dpp v26, v26, v26 quad_perm:[1,0,3,2] row_mask:0xf bank_mask:0xf
	v_max3_f32 v29, v28, s10, v18
	v_cvt_f32_f16_e32 v25, v8
	v_add_f32_dpp v26, v26, v26 quad_perm:[2,3,0,1] row_mask:0xf bank_mask:0xf
	v_add_f32_e32 v19, v19, v15
	v_lshlrev_b32_e32 v71, 4, v69
	v_add_f32_dpp v27, v26, v26 row_half_mirror row_mask:0xf bank_mask:0xf
	v_mov_b32_e32 v31, v27
	v_mov_b32_e32 v26, v14
	s_nop 0
	v_mov_b32_dpp v31, v31 row_mirror row_mask:0xf bank_mask:0xf
	v_pk_add_f32 v[26:27], v[26:27], v[30:31]
	s_nop 0
	v_fmac_f32_e32 v26, v7, v27
	v_mul_f32_e32 v10, 0x3e4ccccd, v26
	v_cmp_lt_f32_e32 vcc, 0, v26
	s_nop 1
	v_cndmask_b32_e32 v14, v10, v26, vcc
	v_cmp_eq_u32_e32 vcc, v69, v35
	s_nop 0
	v_max_f32_dpp v10, v29, v29 quad_perm:[1,0,3,2] row_mask:0xf bank_mask:0xf
	v_cvt_f32_f16_e32 v29, v4
	s_nop 0
	v_max_f32_dpp v10, v10, v10 quad_perm:[2,3,0,1] row_mask:0xf bank_mask:0xf
	s_nop 1
	v_max_f32_dpp v10, v10, v10 row_half_mirror row_mask:0xf bank_mask:0xf
	s_nop 1
	v_max_f32_dpp v26, v10, v10 row_mirror row_mask:0xf bank_mask:0xf
	v_max_f32_e32 v26, v26, v14
	v_sub_f32_e32 v10, v28, v26
	v_mul_f32_e32 v10, 0x3fb8aa3b, v10
	v_exp_f32_e32 v27, v10
	v_sub_f32_e32 v10, v18, v26
	v_mul_f32_e32 v10, 0x3fb8aa3b, v10
	v_exp_f32_e32 v28, v10
	v_cvt_f32_f16_sdwa v10, v8 dst_sel:DWORD dst_unused:UNUSED_PAD src0_sel:WORD_1
	v_add_f32_e32 v8, 0, v27
	v_cndmask_b32_e64 v8, 0, v8, s[2:3]
	v_cndmask_b32_e64 v18, 0, v28, s[4:5]
	v_add_f32_e32 v8, v18, v8
	v_sub_f32_e32 v14, v14, v26
	v_mul_f32_e32 v14, 0x3fb8aa3b, v14
	v_add_f32_dpp v8, v8, v8 quad_perm:[1,0,3,2] row_mask:0xf bank_mask:0xf
	v_exp_f32_e32 v14, v14
	s_nop 0
	v_add_f32_dpp v8, v8, v8 quad_perm:[2,3,0,1] row_mask:0xf bank_mask:0xf
	s_nop 1
	v_add_f32_dpp v8, v8, v8 row_half_mirror row_mask:0xf bank_mask:0xf
	s_nop 1
	v_add_f32_dpp v8, v8, v8 row_mirror row_mask:0xf bank_mask:0xf
	v_add_f32_e32 v8, v14, v8
	v_add_f32_e32 v8, 0x24e69595, v8
	v_rcp_f32_e32 v26, v8
	v_cvt_f32_f16_sdwa v18, v3 dst_sel:DWORD dst_unused:UNUSED_PAD src0_sel:WORD_1
	v_cvt_f32_f16_sdwa v3, v4 dst_sel:DWORD dst_unused:UNUSED_PAD src0_sel:WORD_1
	v_mul_f32_e32 v4, v14, v26
	v_mul_f32_e32 v8, v27, v26
	v_cndmask_b32_e32 v14, 0, v4, vcc
	v_cndmask_b32_e64 v8, v14, v8, s[2:3]
	v_add_f32_e32 v14, v22, v15
	v_add_f32_e32 v14, v14, v32
	v_mul_f32_e32 v22, 0x3e4ccccd, v14
	v_cmp_lt_f32_e64 s[6:7], 0, v14
	v_add_f32_e32 v19, v19, v18
	v_cndmask_b32_e64 v18, 0, v18, s[4:5]
	v_cndmask_b32_e64 v14, v22, v14, s[6:7]
	v_cndmask_b32_e64 v22, v5, v14, s[2:3]
	v_add_f32_e32 v14, 0, v32
	v_cndmask_b32_e64 v14, 0, v14, s[2:3]
	v_add_f32_e32 v14, v14, v18
	v_mul_f32_e32 v27, 0x3e4ccccd, v19
	v_cmp_lt_f32_e64 s[6:7], 0, v19
	v_add_f32_dpp v14, v14, v14 quad_perm:[1,0,3,2] row_mask:0xf bank_mask:0xf
	s_nop 0
	v_cndmask_b32_e64 v19, v27, v19, s[6:7]
	v_cndmask_b32_e64 v27, v5, v19, s[4:5]
	v_add_f32_dpp v14, v14, v14 quad_perm:[2,3,0,1] row_mask:0xf bank_mask:0xf
	v_max3_f32 v30, v22, s10, v27
	s_nop 0
	v_add_f32_dpp v19, v14, v14 row_half_mirror row_mask:0xf bank_mask:0xf
	v_mov_b32_e32 v18, v15
	v_mov_b32_e32 v15, v19
	v_mov_b32_e32 v14, v11
	s_nop 0
	v_mov_b32_dpp v15, v15 row_mirror row_mask:0xf bank_mask:0xf
	v_pk_add_f32 v[14:15], v[18:19], v[14:15]
	s_nop 0
	v_fmac_f32_e32 v14, v7, v15
	v_mul_f32_e32 v11, 0x3e4ccccd, v14
	v_cmp_lt_f32_e64 s[6:7], 0, v14
	s_nop 1
	v_cndmask_b32_e64 v11, v11, v14, s[6:7]
	v_cmp_eq_u32_e64 s[6:7], v9, v35
	s_nop 0
	v_max_f32_dpp v14, v30, v30 quad_perm:[1,0,3,2] row_mask:0xf bank_mask:0xf
	v_cndmask_b32_e64 v4, 0, v4, s[6:7]
	s_nop 0
	v_max_f32_dpp v14, v14, v14 quad_perm:[2,3,0,1] row_mask:0xf bank_mask:0xf
	s_nop 1
	v_max_f32_dpp v14, v14, v14 row_half_mirror row_mask:0xf bank_mask:0xf
	s_nop 1
	v_max_f32_dpp v15, v14, v14 row_mirror row_mask:0xf bank_mask:0xf
	v_max_f32_e32 v14, v15, v11
	v_sub_f32_e32 v15, v22, v14
	v_mul_f32_e32 v15, 0x3fb8aa3b, v15
	v_sub_f32_e32 v18, v27, v14
	v_exp_f32_e32 v15, v15
	v_mul_f32_e32 v18, 0x3fb8aa3b, v18
	v_exp_f32_e32 v27, v18
	v_sub_f32_e32 v11, v11, v14
	v_add_f32_e32 v19, 0, v15
	v_cndmask_b32_e64 v19, 0, v19, s[2:3]
	v_cndmask_b32_e64 v22, 0, v27, s[4:5]
	v_add_f32_e32 v19, v22, v19
	v_mul_f32_e32 v11, 0x3fb8aa3b, v11
	v_exp_f32_e32 v11, v11
	v_add_f32_dpp v14, v19, v19 quad_perm:[1,0,3,2] row_mask:0xf bank_mask:0xf
	v_mul_f32_e32 v18, v28, v26
	v_mov_b32_e32 v22, v12
	v_add_f32_dpp v14, v14, v14 quad_perm:[2,3,0,1] row_mask:0xf bank_mask:0xf
	s_nop 1
	v_add_f32_dpp v14, v14, v14 row_half_mirror row_mask:0xf bank_mask:0xf
	s_nop 1
	v_add_f32_dpp v14, v14, v14 row_mirror row_mask:0xf bank_mask:0xf
	v_add_f32_e32 v14, v11, v14
	v_add_f32_e32 v14, 0x24e69595, v14
	v_rcp_f32_e32 v26, v14
	v_add_f32_e32 v19, v20, v16
	v_cndmask_b32_e64 v14, v4, v18, s[4:5]
	v_add_f32_e32 v19, v19, v29
	v_mul_f32_e32 v9, v15, v26
	v_add_f32_e32 v15, v23, v16
	v_add_f32_e32 v15, v15, v25
	v_mul_f32_e32 v18, 0x3e4ccccd, v15
	v_cmp_lt_f32_e64 s[8:9], 0, v15
	v_mul_f32_e32 v20, 0x3e4ccccd, v19
	v_mul_f32_e32 v4, v11, v26
	v_cndmask_b32_e64 v15, v18, v15, s[8:9]
	v_add_f32_e32 v18, 0, v25
	v_cmp_lt_f32_e64 s[8:9], 0, v19
	v_cndmask_b32_e64 v18, 0, v18, s[2:3]
	v_cndmask_b32_e64 v15, v5, v15, s[2:3]
	v_cndmask_b32_e64 v19, v20, v19, s[8:9]
	v_cndmask_b32_e64 v20, 0, v29, s[4:5]
	v_add_f32_e32 v18, v18, v20
	v_cndmask_b32_e64 v25, v5, v19, s[4:5]
	v_max3_f32 v28, v15, s10, v25
	v_cndmask_b32_e32 v11, 0, v4, vcc
	v_add_f32_dpp v18, v18, v18 quad_perm:[1,0,3,2] row_mask:0xf bank_mask:0xf
	v_cndmask_b32_e64 v9, v11, v9, s[2:3]
	v_cndmask_b32_e64 v4, 0, v4, s[6:7]
	v_add_f32_dpp v18, v18, v18 quad_perm:[2,3,0,1] row_mask:0xf bank_mask:0xf
	s_nop 1
	v_add_f32_dpp v19, v18, v18 row_half_mirror row_mask:0xf bank_mask:0xf
	v_mov_b32_e32 v23, v19
	v_mov_b32_e32 v18, v16
	s_nop 0
	v_mov_b32_dpp v23, v23 row_mirror row_mask:0xf bank_mask:0xf
	v_pk_add_f32 v[18:19], v[18:19], v[22:23]
	v_fmac_f32_e32 v18, v7, v19
	v_mul_f32_e32 v12, 0x3e4ccccd, v18
	v_cmp_lt_f32_e64 s[8:9], 0, v18
	v_max_f32_dpp v16, v28, v28 quad_perm:[1,0,3,2] row_mask:0xf bank_mask:0xf
	s_nop 0
	v_cndmask_b32_e64 v12, v12, v18, s[8:9]
	s_nop 1
	v_max_f32_dpp v16, v16, v16 quad_perm:[2,3,0,1] row_mask:0xf bank_mask:0xf
	s_nop 1
	v_max_f32_dpp v16, v16, v16 row_half_mirror row_mask:0xf bank_mask:0xf
	s_nop 1
	v_max_f32_dpp v18, v16, v16 row_mirror row_mask:0xf bank_mask:0xf
	v_max_f32_e32 v16, v18, v12
	v_sub_f32_e32 v15, v15, v16
	v_mul_f32_e32 v15, 0x3fb8aa3b, v15
	v_exp_f32_e32 v18, v15
	v_sub_f32_e32 v15, v25, v16
	v_mul_f32_e32 v15, 0x3fb8aa3b, v15
	v_exp_f32_e32 v19, v15
	v_add_f32_e32 v11, 0, v18
	v_cndmask_b32_e64 v11, 0, v11, s[2:3]
	v_sub_f32_e32 v12, v12, v16
	v_cndmask_b32_e64 v15, 0, v19, s[4:5]
	v_add_f32_e32 v11, v15, v11
	v_mul_f32_e32 v12, 0x3fb8aa3b, v12
	v_exp_f32_e32 v12, v12
	v_add_f32_dpp v11, v11, v11 quad_perm:[1,0,3,2] row_mask:0xf bank_mask:0xf
	s_nop 1
	v_add_f32_dpp v11, v11, v11 quad_perm:[2,3,0,1] row_mask:0xf bank_mask:0xf
	s_nop 1
	v_add_f32_dpp v11, v11, v11 row_half_mirror row_mask:0xf bank_mask:0xf
	s_nop 1
	v_add_f32_dpp v11, v11, v11 row_mirror row_mask:0xf bank_mask:0xf
	v_add_f32_e32 v11, v12, v11
	v_add_f32_e32 v11, 0x24e69595, v11
	v_rcp_f32_e32 v16, v11
	v_mul_f32_e32 v11, v27, v26
	v_cndmask_b32_e64 v15, v4, v11, s[4:5]
	v_add_f32_e32 v4, v24, v17
	v_add_f32_e32 v4, v4, v10
	v_mul_f32_e32 v11, 0x3e4ccccd, v4
	v_cmp_lt_f32_e64 s[8:9], 0, v4
	v_mul_f32_e32 v12, v12, v16
	v_cndmask_b32_e32 v20, 0, v12, vcc
	v_cndmask_b32_e64 v4, v11, v4, s[8:9]
	v_cndmask_b32_e64 v22, v5, v4, s[2:3]
	v_add_f32_e32 v4, 0, v10
	v_add_f32_e32 v10, v21, v17
	v_cndmask_b32_e64 v4, 0, v4, s[2:3]
	v_add_f32_e32 v10, v10, v3
	v_cndmask_b32_e64 v3, 0, v3, s[4:5]
	v_add_f32_e32 v3, v4, v3
	v_mul_f32_e32 v11, 0x3e4ccccd, v10
	v_cmp_lt_f32_e64 s[8:9], 0, v10
	v_add_f32_dpp v3, v3, v3 quad_perm:[1,0,3,2] row_mask:0xf bank_mask:0xf
	s_nop 0
	v_cndmask_b32_e64 v10, v11, v10, s[8:9]
	v_cndmask_b32_e64 v21, v5, v10, s[4:5]
	v_add_f32_dpp v3, v3, v3 quad_perm:[2,3,0,1] row_mask:0xf bank_mask:0xf
	v_mov_b32_e32 v10, v13
	v_max3_f32 v23, v22, s10, v21
	v_add_f32_dpp v5, v3, v3 row_half_mirror row_mask:0xf bank_mask:0xf
	v_mov_b32_e32 v11, v5
	v_mov_b32_e32 v4, v17
	v_cndmask_b32_e64 v12, 0, v12, s[6:7]
	v_mov_b32_dpp v11, v11 row_mirror row_mask:0xf bank_mask:0xf
	v_pk_add_f32 v[4:5], v[4:5], v[10:11]
	v_mul_f32_e32 v18, v18, v16
	v_fmac_f32_e32 v4, v7, v5
	v_mul_f32_e32 v3, 0x3e4ccccd, v4
	v_cmp_lt_f32_e64 s[8:9], 0, v4
	v_cndmask_b32_e64 v10, v20, v18, s[2:3]
	s_nop 0
	v_cndmask_b32_e64 v3, v3, v4, s[8:9]
	s_nop 1
	v_max_f32_dpp v4, v23, v23 quad_perm:[1,0,3,2] row_mask:0xf bank_mask:0xf
	s_nop 1
	v_max_f32_dpp v4, v4, v4 quad_perm:[2,3,0,1] row_mask:0xf bank_mask:0xf
	s_nop 1
	v_max_f32_dpp v4, v4, v4 row_half_mirror row_mask:0xf bank_mask:0xf
	s_nop 1
	v_max_f32_dpp v5, v4, v4 row_mirror row_mask:0xf bank_mask:0xf
	v_max_f32_e32 v4, v5, v3
	v_sub_f32_e32 v5, v22, v4
	v_mul_f32_e32 v5, 0x3fb8aa3b, v5
	v_sub_f32_e32 v7, v21, v4
	v_exp_f32_e32 v5, v5
	v_mul_f32_e32 v7, 0x3fb8aa3b, v7
	v_exp_f32_e32 v7, v7
	v_sub_f32_e32 v3, v3, v4
	v_add_f32_e32 v11, 0, v5
	v_cndmask_b32_e64 v11, 0, v11, s[2:3]
	v_cndmask_b32_e64 v13, 0, v7, s[4:5]
	v_add_f32_e32 v11, v13, v11
	v_mul_f32_e32 v3, 0x3fb8aa3b, v3
	v_exp_f32_e32 v3, v3
	v_add_f32_dpp v4, v11, v11 quad_perm:[1,0,3,2] row_mask:0xf bank_mask:0xf
	s_nop 1
	v_add_f32_dpp v4, v4, v4 quad_perm:[2,3,0,1] row_mask:0xf bank_mask:0xf
	s_nop 1
	v_add_f32_dpp v4, v4, v4 row_half_mirror row_mask:0xf bank_mask:0xf
	s_nop 1
	v_add_f32_dpp v4, v4, v4 row_mirror row_mask:0xf bank_mask:0xf
	v_add_f32_e32 v4, v3, v4
	v_add_f32_e32 v4, 0x24e69595, v4
	v_rcp_f32_e32 v4, v4
	v_mul_f32_e32 v11, v19, v16
	v_cndmask_b32_e64 v16, v12, v11, s[4:5]
	v_mul_f32_e32 v3, v3, v4
	v_mul_f32_e32 v5, v5, v4
	v_cndmask_b32_e32 v11, 0, v3, vcc
	v_cndmask_b32_e64 v11, v11, v5, s[2:3]
	v_mul_f32_e32 v4, v7, v4
	v_cndmask_b32_e64 v3, 0, v3, s[6:7]
	s_movk_i32 s2, 0x410
	v_cndmask_b32_e64 v17, v3, v4, s[4:5]
	v_mul_lo_u32 v70, v41, s2
	v_lshlrev_b32_e32 v4, 2, v69
	v_add_u32_e32 v3, v70, v71
	v_add_u32_e32 v4, v70, v4
	v_cmp_gt_u32_e32 vcc, 2, v69
	ds_write_b128 v3, v[8:11]
	ds_write_b128 v3, v[14:17] offset:256
	ds_write2_b32 v4, v6, v2 offset0:192 offset1:208
	s_and_saveexec_b64 s[2:3], vcc
	s_cbranch_execz .LBB2_47
	v_mov_b32_e32 v6, 0
	v_mov_b32_e32 v7, v6
	v_mov_b32_e32 v8, v6
	v_mov_b32_e32 v9, v6
	ds_write_b128 v3, v[6:9] offset:512
	ds_write_b32 v4, v34 offset:896

.LBB2_57:
	s_endpgm
	s_nop 0
	s_nop 0
	s_nop 0
	s_nop 0
	s_nop 0
	s_nop 0
	s_nop 0
	s_nop 0
	s_nop 0
	s_nop 0
	s_nop 0
	s_nop 0
	s_nop 0
	s_nop 0
	s_nop 0
	s_nop 0
	s_nop 0
	s_nop 0
	s_nop 0
	s_nop 0
	s_nop 0
	s_nop 0
	s_nop 0
	s_nop 0
	s_nop 0
	s_nop 0
	s_nop 0
	s_nop 0
	s_nop 0
	s_nop 0
	s_nop 0
	s_nop 0
	s_nop 0
	s_nop 0
	s_nop 0
	s_nop 0
	s_nop 0
	s_nop 0
	s_nop 0
	s_endpgm

.LBB3_32:
	s_or_b64 exec, exec, s[6:7]
	v_add_f32_e32 v17, 0, v17
	v_add_f32_e32 v13, v17, v13
	v_add_f32_e32 v9, v13, v9
	v_cvt_f32_i32_e32 v17, v37
	v_max_f32_e32 v22, v11, v11
	v_add_f32_dpp v9, v9, v9 quad_perm:[1,0,3,2] row_mask:0xf bank_mask:0xf
	v_max_f32_e32 v22, 0xff800000, v22
	v_max3_f32 v22, v22, v7, v14
	v_add_f32_dpp v9, v9, v9 quad_perm:[2,3,0,1] row_mask:0xf bank_mask:0xf
	s_nop 1
	v_add_f32_dpp v9, v9, v9 row_half_mirror row_mask:0xf bank_mask:0xf
	v_mov_b32_e32 v13, v9
	s_nop 1
	v_mov_b32_dpp v13, v13 row_mirror row_mask:0xf bank_mask:0xf
	s_waitcnt vmcnt(0)
	v_pk_add_f32 v[8:9], v[8:9], v[12:13]
	v_max_f32_e32 v12, 1.0, v17
	v_div_scale_f32 v13, s[6:7], v12, v12, v9
	v_rcp_f32_e32 v17, v13
	s_movk_i32 s7, 0x180
	s_mov_b32 s6, 0
	v_fma_f32 v23, -v13, v17, 1.0
	v_fmac_f32_e32 v17, v23, v17
	v_div_scale_f32 v23, vcc, v9, v12, v9
	v_mul_f32_e32 v24, v23, v17
	v_fma_f32 v25, -v13, v24, v23
	v_fmac_f32_e32 v24, v25, v17
	v_fma_f32 v13, -v13, v24, v23
	v_div_fmas_f32 v13, v13, v17, v24
	v_div_fixup_f32 v9, v13, v12, v9
	v_add_f32_e32 v8, v8, v9
	v_mul_f32_e32 v9, 0x3e4ccccd, v8
	v_cmp_lt_f32_e32 vcc, 0, v8
	s_nop 1
	v_cndmask_b32_e32 v8, v9, v8, vcc
	v_cmp_eq_u32_e32 vcc, v33, v37
	s_nop 0
	v_max_f32_dpp v9, v22, v22 quad_perm:[1,0,3,2] row_mask:0xf bank_mask:0xf
	s_nop 1
	v_max_f32_dpp v9, v9, v9 quad_perm:[2,3,0,1] row_mask:0xf bank_mask:0xf
	s_nop 1
	v_max_f32_dpp v9, v9, v9 row_half_mirror row_mask:0xf bank_mask:0xf
	s_nop 1
	v_max_f32_dpp v12, v9, v9 row_mirror row_mask:0xf bank_mask:0xf
	v_max_f32_e32 v9, v12, v8
	v_sub_f32_e32 v11, v11, v9
	v_mul_f32_e32 v11, 0x3fb8aa3b, v11
	v_sub_f32_e32 v7, v7, v9
	v_exp_f32_e32 v11, v11
	v_mul_f32_e32 v7, 0x3fb8aa3b, v7
	v_sub_f32_e32 v13, v14, v9
	v_exp_f32_e32 v7, v7
	v_mul_f32_e32 v13, 0x3fb8aa3b, v13
	v_exp_f32_e32 v13, v13
	v_add_f32_e32 v12, 0, v11
	v_cndmask_b32_e64 v12, 0, v12, s[0:1]
	v_cndmask_b32_e64 v14, 0, v7, s[2:3]
	v_add_f32_e32 v12, v12, v14
	v_cndmask_b32_e64 v14, 0, v13, s[4:5]
	v_add_f32_e32 v12, v12, v14
	v_sub_f32_e32 v8, v8, v9
	v_mul_f32_e32 v8, 0x3fb8aa3b, v8
	v_exp_f32_e32 v8, v8
	v_add_f32_dpp v9, v12, v12 quad_perm:[1,0,3,2] row_mask:0xf bank_mask:0xf
	s_nop 1
	v_add_f32_dpp v9, v9, v9 quad_perm:[2,3,0,1] row_mask:0xf bank_mask:0xf
	s_nop 1
	v_add_f32_dpp v9, v9, v9 row_half_mirror row_mask:0xf bank_mask:0xf
	s_nop 1
	v_add_f32_dpp v9, v9, v9 row_mirror row_mask:0xf bank_mask:0xf
	v_add_f32_e32 v9, v8, v9
	v_add_f32_e32 v9, 0x24e69595, v9
	v_rcp_f32_e32 v12, v9
	v_or_b32_e32 v9, s22, v36
	v_mul_lo_u32 v9, v9, s7
	v_or_b32_e32 v17, v9, v38
	v_mul_f32_e32 v22, v8, v12
	v_mul_f32_e32 v8, v12, v11
	v_cndmask_b32_e32 v9, 0, v22, vcc
	v_cmp_eq_u32_e32 vcc, v16, v37
	v_cndmask_b32_e64 v14, v9, v8, s[0:1]
	v_mul_f32_e32 v7, v12, v7
	v_cndmask_b32_e32 v8, 0, v22, vcc
	v_cndmask_b32_e64 v8, v8, v7, s[2:3]
	v_mov_b32_e32 v9, v10
	v_cmp_eq_u32_e32 vcc, v21, v37
	ds_write2_b64 v17, v[14:15], v[8:9] offset1:16
	v_mul_f32_e32 v7, v12, v13
	v_cndmask_b32_e32 v8, 0, v22, vcc
	v_readlane_b32 s0, v37, 0
	v_cndmask_b32_e64 v8, v8, v7, s[4:5]
	v_mov_b32_e32 v9, v6
	s_mul_i32 s7, s22, 0x180
	s_add_i32 s2, s0, 1
	ds_write_b64 v17, v[8:9] offset:256
	s_setprio 3
	v_readlane_b32 s1, v37, 16
	v_readlane_b32 s2, v37, 32
	v_readlane_b32 s3, v37, 48
	v_or_b32_e32 v6, s22, v36
	v_mul_u32_u24_e32 v6, 0x180, v6
	v_mov_b32_e32 v48, 0
	v_mov_b32_e32 v49, 0
	s_max_i32 s0, s0, s1
	s_max_i32 s2, s2, s3
	s_max_i32 s0, s0, s2
	s_add_i32 s0, s0, 4
	s_and_b32 s0, s0, -4
	s_mov_b32 s1, 0
	v_mov_b32_e32 v50, 0
	v_mov_b32_e32 v51, 0
	ds_read2_b64 v[8:11], v6 offset0:0 offset1:1
	ds_read2_b64 v[12:15], v6 offset0:2 offset1:3
	s_waitcnt lgkmcnt(0)
	v_lshl_or_b32 v9, v9, 7, v38
	v_lshl_or_b32 v11, v11, 7, v38
	v_lshl_or_b32 v13, v13, 7, v38
	v_lshl_or_b32 v15, v15, 7, v38
	buffer_load_dwordx2 v[20:21], v9, s[12:15], 0 offen
	buffer_load_dwordx2 v[22:23], v11, s[12:15], 0 offen
	buffer_load_dwordx2 v[24:25], v13, s[12:15], 0 offen
	buffer_load_dwordx2 v[26:27], v15, s[12:15], 0 offen

.LBB3_55:
	s_waitcnt vmcnt(1)
	v_add_f32_e32 v7, v8, v14
	v_add_f32_e32 v7, v13, v7
	v_mul_f32_e32 v14, 0x3e4ccccd, v7
	v_cmp_lt_f32_e32 vcc, 0, v7
	s_nop 1
	v_cndmask_b32_e32 v7, v14, v7, vcc
	s_or_b64 exec, exec, s[6:7]
	v_mov_b32_e32 v14, 0xff800000
	s_and_saveexec_b64 s[6:7], s[4:5]
	s_cbranch_execnz .LBB3_31
	s_branch .LBB3_32
	s_nop 0
	s_nop 0
	s_nop 0
	s_nop 0
	s_nop 0
	s_nop 0
	s_nop 0
	s_nop 0
	s_nop 0
	s_nop 0
	s_nop 0
	s_nop 0
	s_nop 0
	s_nop 0
	s_nop 0
	s_endpgm

_ZN12_GLOBAL__N_17k_pairsEPKDF16_PKiS1_PKfS5_S5_Pf:
	v_lshrrev_b32_e32 v1, 6, v0
	s_load_dwordx8 s[4:11], s[0:1], 0x0
	v_lshl_or_b32 v1, s2, 3, v1
	v_mov_b32_e32 v27, 0
	v_readfirstlane_b32 s2, v1
	v_and_b32_e32 v1, 15, v0
	s_min_i32 s3, s2, 0x30d3
	v_lshlrev_b32_e32 v2, 1, v1
	v_lshl_or_b32 v2, s3, 5, v2
	v_ashrrev_i32_e32 v3, 31, v2
	s_waitcnt lgkmcnt(0)
	v_lshl_add_u64 v[2:3], v[2:3], 2, s[6:7]
	global_load_dwordx2 v[18:19], v[2:3], off nt
	v_lshlrev_b32_e32 v26, 4, v0
	s_movk_i32 s3, 0x2000
	v_lshl_add_u64 v[6:7], s[8:9], 0, v[26:27]
	v_add_co_u32_e32 v6, vcc, s3, v6
	global_load_dwordx4 v[2:5], v26, s[8:9]
	s_nop 0
	v_addc_co_u32_e32 v7, vcc, 0, v7, vcc
	global_load_dwordx4 v[6:9], v[6:7], off
	v_and_b32_e32 v20, 48, v0
	v_mov_b32_e32 v21, v27
	v_lshlrev_b32_e32 v28, 2, v1
	v_and_b32_e32 v27, 63, v0
	v_lshlrev_b32_e32 v50, 4, v27
	s_cmpk_lt_i32 s2, 0x30d4
	v_cmp_gt_u32_e32 vcc, 4, v1
	s_waitcnt vmcnt(2)
	v_ashrrev_i32_e32 v11, 31, v18
	v_mov_b32_e32 v10, v18
	v_lshlrev_b64 v[10:11], 7, v[10:11]
	v_lshl_add_u64 v[10:11], s[4:5], 0, v[10:11]
	v_lshl_add_u64 v[22:23], v[10:11], 0, v[20:21]
	global_load_dwordx4 v[10:13], v[22:23], off
	global_load_dwordx4 v[14:17], v[22:23], off offset:64
	v_ashrrev_i32_e32 v23, 31, v19
	v_mov_b32_e32 v22, v19
	v_lshlrev_b64 v[18:19], 7, v[22:23]
	v_lshl_add_u64 v[18:19], s[4:5], 0, v[18:19]
	v_lshl_add_u64 v[22:23], v[18:19], 0, v[20:21]
	global_load_dwordx4 v[18:21], v[22:23], off
	s_load_dwordx2 s[4:5], s[0:1], 0x20
	global_load_dwordx4 v[22:25], v[22:23], off offset:64
	s_waitcnt lgkmcnt(0)
	global_load_dword v51, v28, s[4:5]
	global_load_dword v52, v28, s[10:11]
	global_load_dword v53, v28, s[4:5] offset:64
	global_load_dword v54, v28, s[10:11] offset:64
	global_load_dword v55, v28, s[4:5] offset:128
	global_load_dword v56, v28, s[10:11] offset:128
	global_load_dword v57, v28, s[10:11] offset:192
	global_load_dword v58, v28, s[4:5] offset:192
	s_waitcnt vmcnt(13)
	ds_write_b128 v26, v[2:5]
	s_waitcnt vmcnt(12)
	ds_write_b128 v26, v[6:9] offset:8192
	s_waitcnt lgkmcnt(0)
	s_barrier
	ds_read_b128 v[2:5], v50
	ds_read_b128 v[6:9], v50 offset:1024
	ds_read_b128 v[26:29], v50 offset:4096
	ds_read_b128 v[30:33], v50 offset:5120
	ds_read_b128 v[34:37], v50 offset:8192
	ds_read_b128 v[38:41], v50 offset:9216
	ds_read_b128 v[42:45], v50 offset:12288
	ds_read_b128 v[46:49], v50 offset:13312
	s_cselect_b64 s[4:5], -1, 0
	s_and_b64 s[4:5], vcc, s[4:5]
	s_waitcnt vmcnt(11) lgkmcnt(7)
	v_mfma_f32_16x16x32_f16 v[2:5], v[10:13], v[2:5], 0
	s_waitcnt lgkmcnt(5)
	v_mfma_f32_16x16x32_f16 v[26:29], v[10:13], v[26:29], 0
	s_waitcnt lgkmcnt(3)
	v_mfma_f32_16x16x32_f16 v[34:37], v[10:13], v[34:37], 0
	s_waitcnt lgkmcnt(1)
	v_mfma_f32_16x16x32_f16 v[10:13], v[10:13], v[42:45], 0
	s_waitcnt vmcnt(10)
	v_mfma_f32_16x16x32_f16 v[2:5], v[14:17], v[6:9], v[2:5]
	v_mfma_f32_16x16x32_f16 v[6:9], v[14:17], v[30:33], v[26:29]
	v_mfma_f32_16x16x32_f16 v[26:29], v[14:17], v[38:41], v[34:37]
	s_waitcnt lgkmcnt(0)
	v_mfma_f32_16x16x32_f16 v[10:13], v[14:17], v[46:49], v[10:13]
	ds_read_b128 v[14:17], v50 offset:2048
	ds_read_b128 v[30:33], v50 offset:3072
	s_waitcnt vmcnt(9) lgkmcnt(1)
	v_mfma_f32_16x16x32_f16 v[2:5], v[18:21], v[14:17], v[2:5]
	ds_read_b128 v[14:17], v50 offset:6144
	ds_read_b128 v[34:37], v50 offset:7168
	s_waitcnt lgkmcnt(1)
	v_mfma_f32_16x16x32_f16 v[6:9], v[18:21], v[14:17], v[6:9]
	ds_read_b128 v[14:17], v50 offset:10240
	ds_read_b128 v[38:41], v50 offset:11264
	s_waitcnt lgkmcnt(1)
	v_mfma_f32_16x16x32_f16 v[14:17], v[18:21], v[14:17], v[26:29]
	s_nop 2
	ds_read_b128 v[26:29], v50 offset:14336
	ds_read_b128 v[42:45], v50 offset:15360
	s_waitcnt lgkmcnt(1)
	v_mfma_f32_16x16x32_f16 v[10:13], v[18:21], v[26:29], v[10:13]
	s_waitcnt vmcnt(8)
	v_mfma_f32_16x16x32_f16 v[2:5], v[22:25], v[30:33], v[2:5]
	v_mfma_f32_16x16x32_f16 v[6:9], v[22:25], v[34:37], v[6:9]
	v_mfma_f32_16x16x32_f16 v[14:17], v[22:25], v[38:41], v[14:17]
	s_waitcnt vmcnt(7)
	s_nop 4
	v_add_f32_e32 v2, v51, v2
	v_add_f32_e32 v3, v51, v3
	v_add_f32_e32 v4, v51, v4
	s_waitcnt lgkmcnt(0)
	v_mfma_f32_16x16x32_f16 v[10:13], v[22:25], v[42:45], v[10:13]
	v_add_f32_e32 v5, v51, v5
	s_waitcnt vmcnt(5)
	v_add_f32_e32 v6, v53, v6
	v_add_f32_e32 v7, v53, v7
	v_add_f32_e32 v8, v53, v8
	v_add_f32_e32 v9, v53, v9
	v_max_f32_e32 v2, 0, v2
	v_max_f32_e32 v3, 0, v3
	v_max_f32_e32 v4, 0, v4
	v_max_f32_e32 v5, 0, v5
	s_waitcnt vmcnt(3)
	v_add_f32_e32 v14, v55, v14
	v_add_f32_e32 v15, v55, v15
	v_add_f32_e32 v16, v55, v16
	v_add_f32_e32 v17, v55, v17
	v_max_f32_e32 v6, 0, v6
	v_max_f32_e32 v7, 0, v7
	v_max_f32_e32 v8, 0, v8
	v_max_f32_e32 v9, 0, v9
	v_fma_f32 v2, v52, v2, 0
	v_fma_f32 v3, v52, v3, 0
	v_fma_f32 v4, v52, v4, 0
	v_fma_f32 v5, v52, v5, 0
	s_waitcnt vmcnt(0)
	v_add_f32_e32 v10, v58, v10
	v_add_f32_e32 v11, v58, v11
	v_add_f32_e32 v12, v58, v12
	v_add_f32_e32 v13, v58, v13
	v_max_f32_e32 v14, 0, v14
	v_max_f32_e32 v15, 0, v15
	v_max_f32_e32 v16, 0, v16
	v_max_f32_e32 v17, 0, v17
	v_fmac_f32_e32 v2, v54, v6
	v_fmac_f32_e32 v3, v54, v7
	v_fmac_f32_e32 v4, v54, v8
	v_fmac_f32_e32 v5, v54, v9
	v_max_f32_e32 v10, 0, v10
	v_max_f32_e32 v11, 0, v11
	v_max_f32_e32 v12, 0, v12
	v_max_f32_e32 v13, 0, v13
	v_fmac_f32_e32 v2, v56, v14
	v_fmac_f32_e32 v3, v56, v15
	v_fmac_f32_e32 v4, v56, v16
	v_fmac_f32_e32 v5, v56, v17
	v_fmac_f32_e32 v2, v57, v10
	v_fmac_f32_e32 v3, v57, v11
	v_fmac_f32_e32 v4, v57, v12
	v_fmac_f32_e32 v5, v57, v13
	v_add_f32_dpp v2, v2, v2 quad_perm:[1,0,3,2] row_mask:0xf bank_mask:0xf
	v_add_f32_dpp v3, v3, v3 quad_perm:[1,0,3,2] row_mask:0xf bank_mask:0xf
	v_add_f32_dpp v4, v4, v4 quad_perm:[1,0,3,2] row_mask:0xf bank_mask:0xf
	v_add_f32_dpp v5, v5, v5 quad_perm:[1,0,3,2] row_mask:0xf bank_mask:0xf
	v_add_f32_dpp v2, v2, v2 quad_perm:[2,3,0,1] row_mask:0xf bank_mask:0xf
	v_add_f32_dpp v3, v3, v3 quad_perm:[2,3,0,1] row_mask:0xf bank_mask:0xf
	v_add_f32_dpp v6, v4, v4 quad_perm:[2,3,0,1] row_mask:0xf bank_mask:0xf
	v_add_f32_dpp v7, v5, v5 quad_perm:[2,3,0,1] row_mask:0xf bank_mask:0xf
	v_add_f32_dpp v2, v2, v2 row_half_mirror row_mask:0xf bank_mask:0xf
	v_add_f32_dpp v4, v3, v3 row_half_mirror row_mask:0xf bank_mask:0xf
	v_add_f32_dpp v5, v6, v6 row_half_mirror row_mask:0xf bank_mask:0xf
	v_add_f32_dpp v7, v7, v7 row_half_mirror row_mask:0xf bank_mask:0xf
	v_mov_b32_e32 v3, v2
	v_mov_b32_e32 v6, v4
	v_mov_b32_e32 v8, v5
	v_mov_b32_e32 v9, v7
	v_mov_b32_dpp v3, v3 row_mirror row_mask:0xf bank_mask:0xf
	v_mov_b32_dpp v6, v6 row_mirror row_mask:0xf bank_mask:0xf
	v_mov_b32_dpp v8, v8 row_mirror row_mask:0xf bank_mask:0xf
	v_mov_b32_dpp v9, v9 row_mirror row_mask:0xf bank_mask:0xf
	s_and_saveexec_b64 s[6:7], s[4:5]
	s_cbranch_execz .LBB4_2
	s_load_dwordx4 s[4:7], s[0:1], 0x28
	v_add_f32_e32 v2, v2, v3
	v_cmp_eq_u32_e32 vcc, 0, v1
	v_bfe_u32 v0, v0, 4, 2
	v_add_f32_e32 v4, v4, v6
	s_waitcnt lgkmcnt(0)
	s_load_dword s0, s[4:5], 0x0
	v_cndmask_b32_e32 v2, 0, v2, vcc
	v_cmp_eq_u32_e32 vcc, 1, v1
	v_add_f32_e32 v5, v5, v8
	s_lshl_b32 s1, s2, 4
	v_cndmask_b32_e32 v2, v2, v4, vcc
	v_cmp_eq_u32_e32 vcc, 2, v1
	v_lshlrev_b32_e32 v0, 2, v0
	v_add_f32_e32 v7, v7, v9
	v_cndmask_b32_e32 v2, v2, v5, vcc
	v_cmp_eq_u32_e32 vcc, 3, v1
	v_or3_b32 v0, s1, v0, v1
	v_ashrrev_i32_e32 v1, 31, v0
	v_cndmask_b32_e32 v2, v2, v7, vcc
	v_lshl_add_u64 v[0:1], v[0:1], 2, s[6:7]
	s_waitcnt lgkmcnt(0)
	v_add_f32_e32 v2, s0, v2
	global_store_dword v[0:1], v2, off
